# attention: batched the serialized partial-output (ysp) read-modify-write loads at the end of the selected and window branches into dead registers with counted vmcnt
# speedup vs baseline: 1.0094x; 1.0094x over previous
.LBB0_898:
	s_or_b64 exec, exec, s[0:1]
	global_load_dwordx4 v[18:21], v[184:185], off
	global_load_dwordx4 v[22:25], v[184:185], off offset:64
	global_load_dwordx4 v[26:29], v[184:185], off offset:128
	global_load_dwordx4 v[30:33], v[184:185], off offset:192
	global_load_dwordx4 v[34:37], v[184:185], off offset:256
	global_load_dwordx4 v[118:121], v[184:185], off offset:320
	global_load_dwordx4 v[128:131], v[184:185], off offset:384
	global_load_dwordx4 v[168:171], v[184:185], off offset:448
	v_readlane_b32 s0, v254, 40
	v_readlane_b32 s1, v254, 41
	s_add_i32 s63, s63, s91
	s_cmpk_lt_i32 s63, 0x400
	v_lshl_add_u64 v[14:15], s[0:1], 0, v[188:189]
	v_lshl_add_u64 v[14:15], v[14:15], 0, v[2:3]
	v_lshl_add_u64 v[14:15], v[14:15], 0, v[6:7]
	s_waitcnt vmcnt(7)
	v_pk_fma_f32 v[10:11], v[84:85], v[4:5], v[20:21] op_sel_hi:[1,0,1]
	v_pk_fma_f32 v[8:9], v[82:83], v[4:5], v[18:19] op_sel_hi:[1,0,1]
	s_nop 0
	v_cvt_pk_bf16_f32 v12, v8, v9
	v_cvt_pk_bf16_f32 v13, v10, v11
	s_nop 0
	s_waitcnt vmcnt(6)
	v_pk_fma_f32 v[6:7], v[80:81], v[4:5], v[24:25] op_sel_hi:[1,0,1]
	v_pk_fma_f32 v[8:9], v[78:79], v[4:5], v[22:23] op_sel_hi:[1,0,1]
	global_store_dwordx2 v[14:15], v[12:13], off
	v_cvt_pk_bf16_f32 v10, v8, v9
	v_cvt_pk_bf16_f32 v11, v6, v7
	s_nop 0
	s_waitcnt vmcnt(6)
	v_pk_fma_f32 v[8:9], v[76:77], v[4:5], v[28:29] op_sel_hi:[1,0,1]
	v_pk_fma_f32 v[6:7], v[74:75], v[4:5], v[26:27] op_sel_hi:[1,0,1]
	global_store_dwordx2 v[14:15], v[10:11], off offset:32
	v_cvt_pk_bf16_f32 v10, v6, v7
	v_cvt_pk_bf16_f32 v11, v8, v9
	s_nop 0
	s_waitcnt vmcnt(6)
	v_pk_fma_f32 v[8:9], v[72:73], v[4:5], v[32:33] op_sel_hi:[1,0,1]
	v_pk_fma_f32 v[6:7], v[70:71], v[4:5], v[30:31] op_sel_hi:[1,0,1]
	global_store_dwordx2 v[14:15], v[10:11], off offset:64
	v_cvt_pk_bf16_f32 v10, v6, v7
	v_cvt_pk_bf16_f32 v11, v8, v9
	s_nop 0
	s_waitcnt vmcnt(6)
	v_pk_fma_f32 v[8:9], v[68:69], v[4:5], v[36:37] op_sel_hi:[1,0,1]
	v_pk_fma_f32 v[6:7], v[66:67], v[4:5], v[34:35] op_sel_hi:[1,0,1]
	global_store_dwordx2 v[14:15], v[10:11], off offset:96
	v_cvt_pk_bf16_f32 v10, v6, v7
	v_cvt_pk_bf16_f32 v11, v8, v9
	s_nop 0
	s_waitcnt vmcnt(6)
	v_pk_fma_f32 v[8:9], v[64:65], v[4:5], v[120:121] op_sel_hi:[1,0,1]
	v_pk_fma_f32 v[6:7], v[62:63], v[4:5], v[118:119] op_sel_hi:[1,0,1]
	global_store_dwordx2 v[14:15], v[10:11], off offset:128
	v_cvt_pk_bf16_f32 v10, v6, v7
	v_cvt_pk_bf16_f32 v11, v8, v9
	s_nop 0
	s_waitcnt vmcnt(6)
	v_pk_fma_f32 v[8:9], v[60:61], v[4:5], v[130:131] op_sel_hi:[1,0,1]
	v_pk_fma_f32 v[6:7], v[58:59], v[4:5], v[128:129] op_sel_hi:[1,0,1]
	global_store_dwordx2 v[14:15], v[10:11], off offset:160
	v_cvt_pk_bf16_f32 v10, v6, v7
	v_cvt_pk_bf16_f32 v11, v8, v9
	s_nop 0
	s_waitcnt vmcnt(6)
	v_pk_fma_f32 v[8:9], v[56:57], v[4:5], v[170:171] op_sel_hi:[1,0,1]
	v_pk_fma_f32 v[4:5], v[54:55], v[4:5], v[168:169] op_sel_hi:[1,0,1]
	global_store_dwordx2 v[14:15], v[10:11], off offset:192
	v_cvt_pk_bf16_f32 v4, v4, v5
	v_cvt_pk_bf16_f32 v5, v8, v9
	global_store_dwordx2 v[14:15], v[4:5], off offset:224
	s_cbranch_scc0 .LBB0_1272

.LBB0_1186:
	s_or_b64 exec, exec, s[0:1]
	global_load_dwordx4 v[128:131], v[182:183], off
	global_load_dwordx4 v[168:171], v[182:183], off offset:64
	global_load_dwordx4 v[200:203], v[182:183], off offset:128
	global_load_dwordx4 v[248:251], v[182:183], off offset:192
	ds_bpermute_b32 v1, v245, v135
	s_waitcnt lgkmcnt(0)
	v_add_f32_e32 v1, v135, v1
	ds_bpermute_b32 v5, v246, v1
	s_waitcnt lgkmcnt(0)
	v_add_f32_e32 v1, v1, v5
	v_cmp_lt_f32_e32 vcc, 0, v1
	s_waitcnt vmcnt(3)
	v_pk_fma_f32 v[116:117], v[116:117], v[118:119], v[130:131] op_sel_hi:[1,0,1]
	v_pk_fma_f32 v[114:115], v[114:115], v[118:119], v[128:129] op_sel_hi:[1,0,1]
	global_store_dwordx4 v[182:183], v[114:117], off
	global_load_dwordx4 v[128:131], v[182:183], off offset:256
	s_waitcnt vmcnt(4)
	v_pk_fma_f32 v[112:113], v[112:113], v[118:119], v[170:171] op_sel_hi:[1,0,1]
	v_pk_fma_f32 v[110:111], v[110:111], v[118:119], v[168:169] op_sel_hi:[1,0,1]
	global_store_dwordx4 v[182:183], v[110:113], off offset:64
	global_load_dwordx4 v[168:171], v[182:183], off offset:320
	s_waitcnt vmcnt(5)
	v_pk_fma_f32 v[108:109], v[108:109], v[118:119], v[202:203] op_sel_hi:[1,0,1]
	v_pk_fma_f32 v[106:107], v[106:107], v[118:119], v[200:201] op_sel_hi:[1,0,1]
	global_store_dwordx4 v[182:183], v[106:109], off offset:128
	global_load_dwordx4 v[200:203], v[182:183], off offset:384
	s_waitcnt vmcnt(6)
	v_pk_fma_f32 v[104:105], v[104:105], v[118:119], v[250:251] op_sel_hi:[1,0,1]
	v_pk_fma_f32 v[102:103], v[102:103], v[118:119], v[248:249] op_sel_hi:[1,0,1]
	global_store_dwordx4 v[182:183], v[102:105], off offset:192
	global_load_dwordx4 v[248:251], v[182:183], off offset:448
	s_waitcnt vmcnt(6)
	v_pk_fma_f32 v[100:101], v[100:101], v[118:119], v[130:131] op_sel_hi:[1,0,1]
	v_pk_fma_f32 v[98:99], v[98:99], v[118:119], v[128:129] op_sel_hi:[1,0,1]
	global_store_dwordx4 v[182:183], v[98:101], off offset:256
	s_nop 0
	s_waitcnt vmcnt(5)
	v_pk_fma_f32 v[96:97], v[96:97], v[118:119], v[170:171] op_sel_hi:[1,0,1]
	v_pk_fma_f32 v[94:95], v[94:95], v[118:119], v[168:169] op_sel_hi:[1,0,1]
	global_store_dwordx4 v[182:183], v[94:97], off offset:320
	s_nop 0
	s_waitcnt vmcnt(4)
	v_pk_fma_f32 v[92:93], v[92:93], v[118:119], v[202:203] op_sel_hi:[1,0,1]
	v_pk_fma_f32 v[90:91], v[90:91], v[118:119], v[200:201] op_sel_hi:[1,0,1]
	global_store_dwordx4 v[182:183], v[90:93], off offset:384
	s_nop 0
	s_waitcnt vmcnt(3)
	v_pk_fma_f32 v[88:89], v[88:89], v[118:119], v[250:251] op_sel_hi:[1,0,1]
	v_pk_fma_f32 v[86:87], v[86:87], v[118:119], v[248:249] op_sel_hi:[1,0,1]
	global_store_dwordx4 v[182:183], v[86:89], off offset:448
	s_and_saveexec_b64 s[0:1], vcc
	s_cbranch_execz .LBB0_1188
	global_load_dword v2, v[192:193], off offset:4
	s_waitcnt vmcnt(0)
	v_div_scale_f32 v5, s[6:7], v1, v1, v2
	v_rcp_f32_e32 v86, v5
	v_div_scale_f32 v87, vcc, v2, v1, v2
	v_fma_f32 v88, -v5, v86, 1.0
	v_fmac_f32_e32 v86, v88, v86
	v_mul_f32_e32 v88, v87, v86
	v_fma_f32 v89, -v5, v88, v87
	v_fmac_f32_e32 v88, v89, v86
	v_fma_f32 v5, -v5, v88, v87
	v_div_fmas_f32 v5, v5, v86, v88
	v_div_fixup_f32 v2, v5, v1, v2
.LBB0_1188:
	s_or_b64 exec, exec, s[0:1]
	global_load_dwordx4 v[128:131], v[184:185], off
	global_load_dwordx4 v[168:171], v[184:185], off offset:64
	global_load_dwordx4 v[200:203], v[184:185], off offset:128
	global_load_dwordx4 v[248:251], v[184:185], off offset:192
	s_cmp_gt_i32 s41, -1
	s_waitcnt vmcnt(3)
	v_pk_fma_f32 v[84:85], v[84:85], v[2:3], v[130:131] op_sel_hi:[1,0,1]
	v_pk_fma_f32 v[82:83], v[82:83], v[2:3], v[128:129] op_sel_hi:[1,0,1]
	global_store_dwordx4 v[184:185], v[82:85], off
	global_load_dwordx4 v[128:131], v[184:185], off offset:256
	s_waitcnt vmcnt(4)
	v_pk_fma_f32 v[80:81], v[80:81], v[2:3], v[170:171] op_sel_hi:[1,0,1]
	v_pk_fma_f32 v[78:79], v[78:79], v[2:3], v[168:169] op_sel_hi:[1,0,1]
	global_store_dwordx4 v[184:185], v[78:81], off offset:64
	global_load_dwordx4 v[168:171], v[184:185], off offset:320
	s_waitcnt vmcnt(5)
	v_pk_fma_f32 v[76:77], v[76:77], v[2:3], v[202:203] op_sel_hi:[1,0,1]
	v_pk_fma_f32 v[74:75], v[74:75], v[2:3], v[200:201] op_sel_hi:[1,0,1]
	global_store_dwordx4 v[184:185], v[74:77], off offset:128
	global_load_dwordx4 v[200:203], v[184:185], off offset:384
	s_waitcnt vmcnt(6)
	v_pk_fma_f32 v[72:73], v[72:73], v[2:3], v[250:251] op_sel_hi:[1,0,1]
	v_pk_fma_f32 v[70:71], v[70:71], v[2:3], v[248:249] op_sel_hi:[1,0,1]
	global_store_dwordx4 v[184:185], v[70:73], off offset:192
	global_load_dwordx4 v[248:251], v[184:185], off offset:448
	s_waitcnt vmcnt(6)
	v_pk_fma_f32 v[68:69], v[68:69], v[2:3], v[130:131] op_sel_hi:[1,0,1]
	v_pk_fma_f32 v[66:67], v[66:67], v[2:3], v[128:129] op_sel_hi:[1,0,1]
	global_store_dwordx4 v[184:185], v[66:69], off offset:256
	s_nop 0
	s_waitcnt vmcnt(5)
	v_pk_fma_f32 v[64:65], v[64:65], v[2:3], v[170:171] op_sel_hi:[1,0,1]
	v_pk_fma_f32 v[62:63], v[62:63], v[2:3], v[168:169] op_sel_hi:[1,0,1]
	global_store_dwordx4 v[184:185], v[62:65], off offset:320
	s_nop 0
	s_waitcnt vmcnt(4)
	v_pk_fma_f32 v[60:61], v[60:61], v[2:3], v[202:203] op_sel_hi:[1,0,1]
	v_pk_fma_f32 v[58:59], v[58:59], v[2:3], v[200:201] op_sel_hi:[1,0,1]
	global_store_dwordx4 v[184:185], v[58:61], off offset:384
	s_nop 0
	s_waitcnt vmcnt(3)
	v_pk_fma_f32 v[56:57], v[56:57], v[2:3], v[250:251] op_sel_hi:[1,0,1]
	v_pk_fma_f32 v[54:55], v[54:55], v[2:3], v[248:249] op_sel_hi:[1,0,1]
	global_store_dwordx4 v[184:185], v[54:57], off offset:448
	s_cbranch_scc0 .LBB0_1251
	s_lshl_b32 s1, s17, 19
	s_lshl_b32 s6, s15, 17
	s_lshl_b32 s0, s16, 12
	s_or_b32 s6, s1, s6
	s_or_b32 s8, s14, 7
	s_or_b32 s9, s14, 3
	s_add_i32 s17, s14, 0xfffffe01
	s_add_i32 s44, s14, 0xfffffe05
	s_add_u32 s0, s88, s0
	s_addc_u32 s1, s89, 0
	s_lshl_b32 s7, s15, 8
	s_add_u32 s7, s0, s7
	s_addc_u32 s18, s1, 0
	s_add_u32 s0, s7, 0xc00
	s_addc_u32 s1, s18, 0
	s_lshl_b32 s15, s15, 22
	s_add_u32 s15, s94, s15
	s_addc_u32 s19, s95, 0
	s_lshl_b32 s16, s16, 1
	s_add_u32 s22, s15, s16
	s_addc_u32 s23, s19, 0
	s_add_u32 s24, s22, 0x1000000
	s_addc_u32 s25, s23, 0
	s_add_u32 s26, s7, 0x800
	s_addc_u32 s27, s18, 0
	s_add_u32 s28, s60, s6
	s_addc_u32 s29, s61, 0
	v_readlane_b32 s18, v255, 7
	v_readlane_b32 s19, v255, 8
	s_add_u32 s30, s18, s6
	s_addc_u32 s31, s19, 0
	s_lshl_b32 s6, s13, 15
	s_add_i32 s15, s6, 0
	s_sub_i32 s6, s14, s10
	s_add_i32 s14, s6, 7
	s_lshr_b32 s6, s67, 6
	s_add_i32 s6, s13, s6
	s_lshl_b32 s6, s6, 6
	s_lshl_b32 s7, s66, 6
	s_sub_i32 s6, s6, s7
	s_lshl_b32 s7, s82, 7
	v_mov_b32_e32 v114, v3
	v_mov_b32_e32 v115, v3
	s_sub_i32 s6, s6, s7
	v_mov_b32_e32 v177, v176
	v_mov_b32_e32 v2, v3
	v_mov_b32_e32 v116, v3
	v_mov_b32_e32 v117, v3
	v_mov_b64_e32 v[110:111], v[114:115]
	v_mov_b64_e32 v[106:107], v[114:115]
	v_mov_b64_e32 v[102:103], v[114:115]
	v_mov_b64_e32 v[98:99], v[114:115]
	v_mov_b64_e32 v[94:95], v[114:115]
	v_mov_b64_e32 v[90:91], v[114:115]
	v_mov_b64_e32 v[86:87], v[114:115]
	v_mov_b64_e32 v[82:83], v[114:115]
	v_mov_b64_e32 v[78:79], v[114:115]
	v_mov_b64_e32 v[74:75], v[114:115]
	v_mov_b64_e32 v[70:71], v[114:115]
	v_mov_b64_e32 v[66:67], v[114:115]
	v_mov_b64_e32 v[62:63], v[114:115]
	v_mov_b64_e32 v[58:59], v[114:115]
	v_mov_b64_e32 v[54:55], v[114:115]
	s_sub_i32 s16, s6, 64
	s_add_i32 s45, s13, 2
	s_add_i32 s46, s41, 1
	s_mov_b32 s47, 0
	v_mov_b64_e32 v[112:113], v[116:117]
	v_mov_b64_e32 v[108:109], v[116:117]
	v_mov_b64_e32 v[104:105], v[116:117]
	v_mov_b64_e32 v[100:101], v[116:117]
	v_mov_b64_e32 v[96:97], v[116:117]
	v_mov_b64_e32 v[92:93], v[116:117]
	v_mov_b64_e32 v[88:89], v[116:117]
	v_mov_b64_e32 v[84:85], v[116:117]
	v_mov_b64_e32 v[80:81], v[116:117]
	v_mov_b64_e32 v[76:77], v[116:117]
	v_mov_b64_e32 v[72:73], v[116:117]
	v_mov_b64_e32 v[68:69], v[116:117]
	v_mov_b64_e32 v[64:65], v[116:117]
	v_mov_b64_e32 v[60:61], v[116:117]
	v_mov_b64_e32 v[56:57], v[116:117]
	v_mov_b64_e32 v[134:135], v[2:3]
	v_mov_b64_e32 v[136:137], v[176:177]
	s_add_i32 s6, s45, -1
	s_cmp_ge_i32 s6, s12
	s_mov_b64 s[6:7], -1
	s_cbranch_scc0 .LBB0_1192
	s_branch .LBB0_1191

.LBB0_1254:
	s_or_b64 exec, exec, s[0:1]
	global_load_dwordx4 v[18:21], v[182:183], off
	global_load_dwordx4 v[22:25], v[182:183], off offset:64
	global_load_dwordx4 v[26:29], v[182:183], off offset:128
	global_load_dwordx4 v[30:33], v[182:183], off offset:192
	global_load_dwordx4 v[34:37], v[182:183], off offset:256
	global_load_dwordx4 v[118:121], v[182:183], off offset:320
	global_load_dwordx4 v[128:131], v[182:183], off offset:384
	global_load_dwordx4 v[168:171], v[182:183], off offset:448
	v_readlane_b32 s0, v254, 40
	v_readlane_b32 s1, v254, 41
	v_lshlrev_b32_e32 v2, 1, v178
	ds_bpermute_b32 v1, v245, v135
	v_lshl_add_u64 v[16:17], s[0:1], 0, v[186:187]
	v_lshl_add_u64 v[16:17], v[16:17], 0, v[2:3]
	s_waitcnt lgkmcnt(0)
	v_add_f32_e32 v1, v135, v1
	ds_bpermute_b32 v5, v246, v1
	s_waitcnt lgkmcnt(0)
	v_add_f32_e32 v1, v1, v5
	v_cmp_lt_f32_e32 vcc, 0, v1
	s_waitcnt vmcnt(7)
	v_pk_fma_f32 v[10:11], v[114:115], v[8:9], v[18:19] op_sel_hi:[1,0,1]
	v_pk_fma_f32 v[6:7], v[116:117], v[8:9], v[20:21] op_sel_hi:[1,0,1]
	v_cvt_pk_bf16_f32 v14, v10, v11
	s_nop 0
	v_cvt_pk_bf16_f32 v15, v6, v7
	s_nop 0
	v_lshlrev_b32_e32 v6, 1, v216
	v_mov_b32_e32 v7, v3
	v_lshl_add_u64 v[16:17], v[16:17], 0, v[6:7]
	global_store_dwordx2 v[16:17], v[14:15], off
	s_waitcnt vmcnt(7)
	v_pk_fma_f32 v[12:13], v[112:113], v[8:9], v[24:25] op_sel_hi:[1,0,1]
	v_pk_fma_f32 v[10:11], v[110:111], v[8:9], v[22:23] op_sel_hi:[1,0,1]
	s_nop 0
	v_cvt_pk_bf16_f32 v14, v10, v11
	v_cvt_pk_bf16_f32 v15, v12, v13
	s_nop 0
	s_waitcnt vmcnt(6)
	v_pk_fma_f32 v[12:13], v[108:109], v[8:9], v[28:29] op_sel_hi:[1,0,1]
	v_pk_fma_f32 v[10:11], v[106:107], v[8:9], v[26:27] op_sel_hi:[1,0,1]
	global_store_dwordx2 v[16:17], v[14:15], off offset:32
	v_cvt_pk_bf16_f32 v14, v10, v11
	v_cvt_pk_bf16_f32 v15, v12, v13
	s_nop 0
	s_waitcnt vmcnt(6)
	v_pk_fma_f32 v[12:13], v[104:105], v[8:9], v[32:33] op_sel_hi:[1,0,1]
	v_pk_fma_f32 v[10:11], v[102:103], v[8:9], v[30:31] op_sel_hi:[1,0,1]
	global_store_dwordx2 v[16:17], v[14:15], off offset:64
	v_cvt_pk_bf16_f32 v14, v10, v11
	v_cvt_pk_bf16_f32 v15, v12, v13
	s_nop 0
	s_waitcnt vmcnt(6)
	v_pk_fma_f32 v[12:13], v[100:101], v[8:9], v[36:37] op_sel_hi:[1,0,1]
	v_pk_fma_f32 v[10:11], v[98:99], v[8:9], v[34:35] op_sel_hi:[1,0,1]
	global_store_dwordx2 v[16:17], v[14:15], off offset:96
	v_cvt_pk_bf16_f32 v14, v10, v11
	v_cvt_pk_bf16_f32 v15, v12, v13
	s_nop 0
	s_waitcnt vmcnt(6)
	v_pk_fma_f32 v[12:13], v[96:97], v[8:9], v[120:121] op_sel_hi:[1,0,1]
	v_pk_fma_f32 v[10:11], v[94:95], v[8:9], v[118:119] op_sel_hi:[1,0,1]
	global_store_dwordx2 v[16:17], v[14:15], off offset:128
	v_cvt_pk_bf16_f32 v14, v10, v11
	v_cvt_pk_bf16_f32 v15, v12, v13
	s_nop 0
	s_waitcnt vmcnt(6)
	v_pk_fma_f32 v[12:13], v[92:93], v[8:9], v[130:131] op_sel_hi:[1,0,1]
	v_pk_fma_f32 v[10:11], v[90:91], v[8:9], v[128:129] op_sel_hi:[1,0,1]
	global_store_dwordx2 v[16:17], v[14:15], off offset:160
	v_cvt_pk_bf16_f32 v14, v10, v11
	v_cvt_pk_bf16_f32 v15, v12, v13
	s_nop 0
	s_waitcnt vmcnt(6)
	v_pk_fma_f32 v[12:13], v[88:89], v[8:9], v[170:171] op_sel_hi:[1,0,1]
	v_pk_fma_f32 v[8:9], v[86:87], v[8:9], v[168:169] op_sel_hi:[1,0,1]
	global_store_dwordx2 v[16:17], v[14:15], off offset:192
	v_cvt_pk_bf16_f32 v8, v8, v9
	v_cvt_pk_bf16_f32 v9, v12, v13
	global_store_dwordx2 v[16:17], v[8:9], off offset:224
	s_and_saveexec_b64 s[0:1], vcc
	s_cbranch_execz .LBB0_898
	global_load_dword v4, v[192:193], off offset:8
	s_waitcnt vmcnt(0)
	v_div_scale_f32 v5, s[6:7], v1, v1, v4
	v_rcp_f32_e32 v8, v5
	v_div_scale_f32 v9, vcc, v4, v1, v4
	v_fma_f32 v10, -v5, v8, 1.0
	v_fmac_f32_e32 v8, v10, v8
	v_mul_f32_e32 v10, v9, v8
	v_fma_f32 v11, -v5, v10, v9
	v_fmac_f32_e32 v10, v11, v8
	v_fma_f32 v5, -v5, v10, v9
	v_div_fmas_f32 v5, v5, v8, v10
	v_div_fixup_f32 v4, v5, v1, v4
	s_branch .LBB0_898
